# P9 token loop: non-temporal hint on the row loads and the output stores
# baseline (speedup 1.0000x reference)
.LBB0_1205:
	s_add_i32 s1, s9, -3
	s_add_i32 s2, s9, -2
	s_add_i32 s3, s9, -1
	v_readlane_b32 s0, v130, s9
	v_readlane_b32 s24, v130, s1
	v_readlane_b32 s2, v130, s2
	v_readlane_b32 s26, v130, s3
	v_lshl_add_u64 v[0:1], s[92:93], 0, v[106:107]
	s_ashr_i32 s1, s0, 31
	s_ashr_i32 s25, s24, 31
	s_ashr_i32 s3, s2, 31
	s_ashr_i32 s27, s26, 31
	v_add_co_u32_e32 v0, vcc, s11, v0
	s_add_u32 s28, s92, s21
	v_mov_b32_e32 v6, 0
	v_addc_co_u32_e32 v1, vcc, 0, v1, vcc
	s_addc_u32 s29, s93, s22
	s_lshl_b64 s[24:25], s[24:25], 11
	v_lshl_add_u64 v[2:3], s[92:93], 0, v[110:111]
	v_lshl_add_u64 v[4:5], s[92:93], 0, v[108:109]
	s_lshl_b64 s[2:3], s[2:3], 11
	s_lshl_b64 s[26:27], s[26:27], 11
	s_lshl_b64 s[0:1], s[0:1], 11
	global_load_dwordx2 v[212:213], v126, s[28:29]
	global_load_dwordx4 v[132:135], v[0:1], off nt
	global_load_dwordx4 v[136:139], v[2:3], off nt
	global_load_dwordx4 v[140:143], v[0:1], off offset:2048 nt
	global_load_dwordx4 v[144:147], v[4:5], off nt
	v_lshl_add_u64 v[0:1], v[112:113], 0, s[24:25]
	v_lshl_add_u64 v[2:3], v[112:113], 0, s[2:3]
	v_lshl_add_u64 v[4:5], v[112:113], 0, s[26:27]
	v_lshl_add_u64 v[8:9], v[112:113], 0, s[0:1]
	global_load_dwordx4 v[92:95], v[0:1], off nt
	global_load_dwordx4 v[88:91], v[2:3], off nt
	global_load_dwordx4 v[84:87], v[4:5], off nt
	global_load_dwordx4 v[80:83], v[8:9], off nt
	global_load_dwordx4 v[76:79], v[0:1], off offset:1024 nt
	global_load_dwordx4 v[72:75], v[2:3], off offset:1024 nt
	global_load_dwordx4 v[68:71], v[4:5], off offset:1024 nt
	global_load_dwordx4 v[64:67], v[8:9], off offset:1024 nt
	v_lshl_add_u32 v44, v6, 2, v129
	ds_read_b128 v[148:151], v44
	ds_read_b128 v[152:155], v44 offset:1024
	ds_read_b128 v[156:159], v44 offset:8192
	ds_read_b128 v[160:163], v44 offset:9216
	ds_read_b128 v[164:167], v44 offset:2048
	ds_read_b128 v[168:171], v44 offset:3072
	ds_read_b128 v[172:175], v44 offset:10240
	ds_read_b128 v[176:179], v44 offset:11264
	ds_read_b128 v[180:183], v44 offset:4096
	ds_read_b128 v[184:187], v44 offset:5120
	ds_read_b128 v[188:191], v44 offset:12288
	ds_read_b128 v[192:195], v44 offset:13312
	ds_read_b128 v[196:199], v44 offset:6144
	ds_read_b128 v[200:203], v44 offset:7168
	ds_read_b128 v[204:207], v44 offset:14336
	ds_read_b128 v[208:211], v44 offset:15360
	ds_read_b128 v[16:19], v44 offset:16384
	ds_read_b128 v[0:3], v44 offset:17408
	ds_read_b128 v[48:51], v44 offset:24576
	ds_read_b128 v[32:35], v44 offset:25600
	ds_read_b128 v[20:23], v44 offset:18432
	ds_read_b128 v[4:7], v44 offset:19456
	ds_read_b128 v[52:55], v44 offset:26624
	ds_read_b128 v[36:39], v44 offset:27648
	ds_read_b128 v[24:27], v44 offset:20480
	ds_read_b128 v[8:11], v44 offset:21504
	ds_read_b128 v[56:59], v44 offset:28672
	ds_read_b128 v[40:43], v44 offset:29696
	ds_read_b128 v[28:31], v44 offset:22528
	ds_read_b128 v[12:15], v44 offset:23552
	ds_read_b128 v[60:63], v44 offset:30720
	ds_read_b128 v[44:47], v44 offset:31744
	s_add_u32 s4, s4, s6
	s_addc_u32 s5, s5, s7
	s_add_i32 s9, s9, 4
	s_add_u32 s21, s21, s12
	s_addc_u32 s22, s22, s13
	v_lshl_add_u64 v[116:117], s[16:17], 0, v[96:97]
	v_lshl_add_u64 v[118:119], s[16:17], 0, v[98:99]
	v_lshl_add_u64 v[120:121], s[16:17], 0, v[100:101]
	v_lshl_add_u64 v[122:123], s[16:17], 0, v[102:103]
	v_lshl_add_u64 v[124:125], s[16:17], 0, v[104:105]
	v_cmp_lt_u64_e32 vcc, s[4:5], v[114:115]
	s_add_u32 s16, s16, s18
	s_addc_u32 s17, s17, s19
	s_and_b64 s[0:1], exec, vcc
	v_lshl_add_u64 v[108:109], v[108:109], 0, s[14:15]
	v_lshl_add_u64 v[106:107], v[106:107], 0, s[14:15]
	v_lshl_add_u64 v[110:111], v[110:111], 0, s[14:15]
	s_waitcnt vmcnt(11)
	v_mov_b32_e32 v131, v134
	v_mov_b32_e32 v134, v135
	s_nop 0
	v_permlane16_swap_b32_e32 v132, v131
	s_waitcnt vmcnt(10)
	v_mov_b32_e32 v135, v138
	v_permlane16_swap_b32_e32 v133, v134
	s_waitcnt vmcnt(7)
	v_mov_b32_e32 v230, v93
	s_waitcnt vmcnt(2)
	v_mov_b32_e32 v235, v73
	s_waitcnt vmcnt(1)
	v_mov_b32_e32 v236, v69
	s_waitcnt vmcnt(0)
	v_mov_b32_e32 v237, v67
	v_lshlrev_b32_e32 v67, 16, v132
	v_and_b32_e32 v69, 0xffff0000, v132
	v_mov_b32_e32 v138, v139
	v_mov_b32_e32 v139, v142
	v_mov_b32_e32 v142, v143
	v_mov_b32_e32 v143, v146
	v_mov_b32_e32 v146, v147
	v_permlane16_swap_b32_e32 v136, v135
	v_mov_b32_e32 v231, v89
	v_mov_b32_e32 v234, v79
	v_lshlrev_b32_e32 v73, 16, v133
	v_and_b32_e32 v79, 0xffff0000, v133
	v_permlane16_swap_b32_e32 v92, v230
	v_permlane16_swap_b32_e32 v94, v95
	v_permlane16_swap_b32_e32 v72, v235
	v_sub_f32_e32 v133, v69, v212
	v_sub_f32_e32 v132, v67, v212
	v_permlane16_swap_b32_e32 v137, v138
	v_permlane16_swap_b32_e32 v140, v139
	v_permlane16_swap_b32_e32 v141, v142
	v_permlane16_swap_b32_e32 v144, v143
	v_permlane16_swap_b32_e32 v145, v146
	v_lshlrev_b32_e32 v89, 16, v134
	v_and_b32_e32 v93, 0xffff0000, v134
	v_lshlrev_b32_e32 v216, 16, v135
	v_and_b32_e32 v217, 0xffff0000, v135
	v_permlane16_swap_b32_e32 v88, v231
	v_permlane16_swap_b32_e32 v90, v91
	v_permlane16_swap_b32_e32 v68, v236
	v_permlane16_swap_b32_e32 v66, v237
	v_sub_f32_e32 v135, v79, v212
	v_sub_f32_e32 v134, v73, v212
	v_permlane32_swap_b32_e32 v230, v95
	v_mov_b32_e32 v250, v72
	v_pk_mul_f32 v[72:73], v[212:213], v[132:133] op_sel:[1,0]
	v_mov_b32_e32 v232, v87
	v_mov_b32_e32 v233, v83
	v_lshlrev_b32_e32 v83, 16, v131
	v_and_b32_e32 v87, 0xffff0000, v131
	v_lshlrev_b32_e32 v131, 16, v136
	v_and_b32_e32 v147, 0xffff0000, v136
	v_lshlrev_b32_e32 v214, 16, v137
	v_and_b32_e32 v215, 0xffff0000, v137
	v_lshlrev_b32_e32 v218, 16, v138
	v_and_b32_e32 v219, 0xffff0000, v138
	v_lshlrev_b32_e32 v220, 16, v140
	v_and_b32_e32 v221, 0xffff0000, v140
	v_lshlrev_b32_e32 v222, 16, v141
	v_and_b32_e32 v223, 0xffff0000, v141
	v_lshlrev_b32_e32 v224, 16, v139
	v_and_b32_e32 v225, 0xffff0000, v139
	v_lshlrev_b32_e32 v228, 16, v144
	v_and_b32_e32 v229, 0xffff0000, v144
	v_lshlrev_b32_e32 v238, 16, v145
	v_and_b32_e32 v239, 0xffff0000, v145
	v_lshlrev_b32_e32 v240, 16, v143
	v_and_b32_e32 v241, 0xffff0000, v143
	v_permlane32_swap_b32_e32 v231, v91
	v_mov_b32_e32 v251, v68
	v_pk_mul_f32 v[68:69], v[212:213], v[134:135] op_sel:[1,0]
	v_mov_b32_e32 v252, v66
	s_waitcnt lgkmcnt(14)
	v_pk_fma_f32 v[66:67], v[72:73], v[148:149], v[156:157]
	v_cvt_pk_f32_fp8_e32 v[72:73], v230
	v_lshlrev_b32_e32 v226, 16, v142
	v_and_b32_e32 v227, 0xffff0000, v142
	v_lshlrev_b32_e32 v242, 16, v146
	v_and_b32_e32 v243, 0xffff0000, v146
	v_permlane16_swap_b32_e32 v86, v232
	v_permlane16_swap_b32_e32 v82, v233
	v_permlane16_swap_b32_e32 v76, v77
	v_permlane16_swap_b32_e32 v78, v234
	v_sub_f32_e32 v137, v87, v212
	v_sub_f32_e32 v136, v83, v212
	v_sub_f32_e32 v141, v215, v212
	v_sub_f32_e32 v140, v214, v212
	v_sub_f32_e32 v143, v147, v212
	v_sub_f32_e32 v142, v131, v212
	v_sub_f32_e32 v145, v219, v212
	v_sub_f32_e32 v144, v218, v212
	v_sub_f32_e32 v147, v217, v212
	v_sub_f32_e32 v146, v216, v212
	v_sub_f32_e32 v215, v221, v212
	v_sub_f32_e32 v214, v220, v212
	v_sub_f32_e32 v217, v223, v212
	v_sub_f32_e32 v216, v222, v212
	v_sub_f32_e32 v219, v225, v212
	v_sub_f32_e32 v218, v224, v212
	v_sub_f32_e32 v223, v239, v212
	v_sub_f32_e32 v222, v238, v212
	v_sub_f32_e32 v225, v229, v212
	v_sub_f32_e32 v224, v228, v212
	v_sub_f32_e32 v229, v241, v212
	v_sub_f32_e32 v228, v240, v212
	v_mov_b32_e32 v131, v92
	v_pk_fma_f32 v[68:69], v[68:69], v[150:151], v[158:159]
	v_cvt_pk_f32_fp8_sdwa v[148:149], v230 src0_sel:WORD_1
	v_cvt_pk_f32_fp8_e32 v[158:159], v231
	v_permlane16_swap_b32_e32 v84, v85
	v_permlane16_swap_b32_e32 v80, v81
	v_permlane16_swap_b32_e32 v74, v75
	v_permlane16_swap_b32_e32 v70, v71
	v_permlane16_swap_b32_e32 v64, v65
	v_sub_f32_e32 v139, v93, v212
	v_sub_f32_e32 v138, v89, v212
	v_sub_f32_e32 v221, v227, v212
	v_sub_f32_e32 v220, v226, v212
	v_sub_f32_e32 v227, v243, v212
	v_sub_f32_e32 v226, v242, v212
	v_mov_b32_e32 v238, v88
	v_mov_b32_e32 v239, v86
	v_mov_b32_e32 v240, v82
	v_mov_b32_e32 v241, v78
	v_permlane32_swap_b32_e32 v77, v234
	v_pk_mul_f32 v[82:83], v[212:213], v[136:137] op_sel:[1,0]
	v_pk_mul_f32 v[92:93], v[212:213], v[146:147] op_sel:[1,0]
	v_pk_mul_f32 v[132:133], v[212:213], v[144:145] op_sel:[1,0]
	v_pk_mul_f32 v[136:137], v[212:213], v[214:215] op_sel:[1,0]
	v_pk_mul_f32 v[144:145], v[212:213], v[222:223] op_sel:[1,0]
	v_pk_mul_f32 v[146:147], v[212:213], v[228:229] op_sel:[1,0]
	v_permlane32_swap_b32_e32 v131, v94
	v_cvt_pk_f32_fp8_sdwa v[214:215], v231 src0_sel:WORD_1
	v_permlane32_swap_b32_e32 v85, v232
	v_permlane32_swap_b32_e32 v81, v233
	v_permlane32_swap_b32_e32 v235, v75
	v_permlane32_swap_b32_e32 v236, v71
	v_pk_mul_f32 v[78:79], v[212:213], v[138:139] op_sel:[1,0]
	v_pk_mul_f32 v[86:87], v[212:213], v[142:143] op_sel:[1,0]
	v_pk_mul_f32 v[88:89], v[212:213], v[140:141] op_sel:[1,0]
	v_pk_mul_f32 v[134:135], v[212:213], v[216:217] op_sel:[1,0]
	v_pk_mul_f32 v[138:139], v[212:213], v[220:221] op_sel:[1,0]
	v_pk_mul_f32 v[140:141], v[212:213], v[218:219] op_sel:[1,0]
	v_pk_mul_f32 v[142:143], v[212:213], v[224:225] op_sel:[1,0]
	v_pk_mul_f32 v[212:213], v[212:213], v[226:227] op_sel:[1,0]
	v_permlane32_swap_b32_e32 v65, v237
	v_cvt_pk_f32_fp8_e32 v[150:151], v95
	v_cvt_pk_f32_fp8_sdwa v[156:157], v95 src0_sel:WORD_1
	v_permlane32_swap_b32_e32 v238, v90
	v_permlane32_swap_b32_e32 v84, v239
	v_permlane32_swap_b32_e32 v80, v240
	v_permlane32_swap_b32_e32 v76, v241
	v_pk_fma_f32 v[132:133], v[132:133], v[170:171], v[178:179]
	v_pk_fma_f32 v[92:93], v[92:93], v[168:169], v[176:177]
	v_cvt_pk_f32_fp8_e32 v[168:169], v77
	v_cvt_pk_f32_fp8_sdwa v[170:171], v77 src0_sel:WORD_1
	v_cvt_pk_f32_fp8_e32 v[176:177], v234
	v_cvt_pk_f32_fp8_sdwa v[178:179], v234 src0_sel:WORD_1
	v_pk_fma_f32 v[144:145], v[144:145], v[198:199], v[206:207]
	v_pk_fma_f32 v[146:147], v[146:147], v[200:201], v[208:209]
	v_cvt_pk_f32_fp8_e32 v[198:199], v131
	v_cvt_pk_f32_fp8_sdwa v[200:201], v131 src0_sel:WORD_1
	v_pk_fma_f32 v[82:83], v[82:83], v[152:153], v[160:161]
	v_pk_fma_f32 v[78:79], v[78:79], v[154:155], v[162:163]
	v_cvt_pk_f32_fp8_e32 v[152:153], v91
	v_cvt_pk_f32_fp8_sdwa v[154:155], v91 src0_sel:WORD_1
	v_cvt_pk_f32_fp8_e32 v[216:217], v232
	v_pk_fma_f32 v[88:89], v[88:89], v[166:167], v[174:175]
	v_pk_fma_f32 v[86:87], v[86:87], v[164:165], v[172:173]
	v_cvt_pk_f32_fp8_sdwa v[164:165], v232 src0_sel:WORD_1
	v_cvt_pk_f32_fp8_e32 v[174:175], v233
	v_cvt_pk_f32_fp8_sdwa v[218:219], v233 src0_sel:WORD_1
	v_permlane32_swap_b32_e32 v250, v74
	v_cvt_pk_f32_fp8_e32 v[220:221], v235
	v_cvt_pk_f32_fp8_sdwa v[222:223], v235 src0_sel:WORD_1
	v_pk_fma_f32 v[136:137], v[136:137], v[180:181], v[188:189]
	v_pk_fma_f32 v[134:135], v[134:135], v[182:183], v[190:191]
	v_cvt_pk_f32_fp8_e32 v[180:181], v75
	v_cvt_pk_f32_fp8_sdwa v[182:183], v75 src0_sel:WORD_1
	v_cvt_pk_f32_fp8_e32 v[188:189], v236
	v_cvt_pk_f32_fp8_sdwa v[190:191], v236 src0_sel:WORD_1
	v_pk_fma_f32 v[138:139], v[138:139], v[186:187], v[194:195]
	v_cvt_pk_f32_fp8_e32 v[194:195], v237
	v_cvt_pk_f32_fp8_sdwa v[226:227], v237 src0_sel:WORD_1
	v_pk_fma_f32 v[142:143], v[142:143], v[196:197], v[204:205]
	v_pk_fma_f32 v[196:197], v[212:213], v[202:203], v[210:211]
	v_cvt_pk_f32_fp8_e32 v[202:203], v94
	v_cvt_pk_f32_fp8_sdwa v[94:95], v94 src0_sel:WORD_1
	v_cvt_pk_f32_fp8_e32 v[204:205], v238
	v_cvt_pk_f32_fp8_sdwa v[206:207], v238 src0_sel:WORD_1
	v_cvt_pk_f32_fp8_e32 v[212:213], v239
	v_cvt_pk_f32_fp8_sdwa v[228:229], v239 src0_sel:WORD_1
	v_cvt_pk_f32_fp8_e32 v[232:233], v240
	v_cvt_pk_f32_fp8_sdwa v[234:235], v240 src0_sel:WORD_1
	v_cvt_pk_f32_fp8_e32 v[236:237], v76
	v_cvt_pk_f32_fp8_sdwa v[76:77], v76 src0_sel:WORD_1
	v_cvt_pk_f32_fp8_e32 v[238:239], v241
	v_cvt_pk_f32_fp8_sdwa v[240:241], v241 src0_sel:WORD_1
	v_pk_add_f32 v[72:73], v[72:73], 0 op_sel_hi:[1,0]
	v_cvt_pk_f32_fp8_e32 v[160:161], v85
	v_cvt_pk_f32_fp8_sdwa v[162:163], v85 src0_sel:WORD_1
	v_permlane32_swap_b32_e32 v251, v70
	v_cvt_pk_f32_fp8_e32 v[224:225], v71
	v_pk_fma_f32 v[140:141], v[140:141], v[184:185], v[192:193]
	v_cvt_pk_f32_fp8_sdwa v[184:185], v71 src0_sel:WORD_1
	v_cvt_pk_f32_fp8_e32 v[208:209], v90
	v_cvt_pk_f32_fp8_sdwa v[90:91], v90 src0_sel:WORD_1
	v_cvt_pk_f32_fp8_e32 v[210:211], v84
	v_cvt_pk_f32_fp8_sdwa v[84:85], v84 src0_sel:WORD_1
	v_cvt_pk_f32_fp8_e32 v[242:243], v74
	v_cvt_pk_f32_fp8_sdwa v[74:75], v74 src0_sel:WORD_1
	v_cvt_pk_f32_fp8_e32 v[248:249], v250
	v_pk_add_f32 v[72:73], v[72:73], v[158:159]
	v_cvt_pk_f32_fp8_sdwa v[158:159], v250 src0_sel:WORD_1
	v_pk_add_f32 v[148:149], v[148:149], 0 op_sel_hi:[1,0]
	v_cvt_pk_f32_fp8_e32 v[166:167], v81
	v_cvt_pk_f32_fp8_sdwa v[172:173], v81 src0_sel:WORD_1
	v_permlane32_swap_b32_e32 v64, v252
	v_cvt_pk_f32_fp8_e32 v[186:187], v65
	v_cvt_pk_f32_fp8_sdwa v[192:193], v65 src0_sel:WORD_1
	v_cvt_pk_f32_fp8_e32 v[230:231], v80
	v_cvt_pk_f32_fp8_sdwa v[80:81], v80 src0_sel:WORD_1
	v_cvt_pk_f32_fp8_e32 v[244:245], v70
	v_cvt_pk_f32_fp8_sdwa v[70:71], v70 src0_sel:WORD_1
	v_pk_add_f32 v[148:149], v[148:149], v[214:215]
	v_cvt_pk_f32_fp8_e32 v[214:215], v251
	v_cvt_pk_f32_fp8_sdwa v[250:251], v251 src0_sel:WORD_1
	v_cvt_pk_f32_fp8_e32 v[246:247], v64
	v_cvt_pk_f32_fp8_sdwa v[64:65], v64 src0_sel:WORD_1
	v_pk_add_f32 v[150:151], v[150:151], 0 op_sel_hi:[1,0]
	v_pk_add_f32 v[156:157], v[156:157], 0 op_sel_hi:[1,0]
	v_pk_add_f32 v[168:169], v[168:169], 0 op_sel_hi:[1,0]
	v_pk_add_f32 v[170:171], v[170:171], 0 op_sel_hi:[1,0]
	v_pk_add_f32 v[176:177], v[176:177], 0 op_sel_hi:[1,0]
	v_pk_add_f32 v[178:179], v[178:179], 0 op_sel_hi:[1,0]
	v_pk_add_f32 v[198:199], v[198:199], 0 op_sel_hi:[1,0]
	v_pk_add_f32 v[200:201], v[200:201], 0 op_sel_hi:[1,0]
	v_pk_add_f32 v[150:151], v[150:151], v[152:153]
	v_pk_add_f32 v[154:155], v[156:157], v[154:155]
	v_pk_add_f32 v[202:203], v[202:203], 0 op_sel_hi:[1,0]
	v_pk_add_f32 v[94:95], v[94:95], 0 op_sel_hi:[1,0]
	v_pk_add_f32 v[236:237], v[236:237], 0 op_sel_hi:[1,0]
	v_pk_add_f32 v[76:77], v[76:77], 0 op_sel_hi:[1,0]
	v_pk_add_f32 v[240:241], v[240:241], 0 op_sel_hi:[1,0]
	v_pk_add_f32 v[168:169], v[168:169], v[220:221]
	v_pk_add_f32 v[170:171], v[170:171], v[222:223]
	v_pk_add_f32 v[176:177], v[176:177], v[180:181]
	v_pk_add_f32 v[178:179], v[178:179], v[182:183]
	v_pk_add_f32 v[180:181], v[198:199], v[204:205]
	v_pk_add_f32 v[182:183], v[200:201], v[206:207]
	v_pk_add_f32 v[198:199], v[202:203], v[208:209]
	v_pk_add_f32 v[90:91], v[94:95], v[90:91]
	v_pk_add_f32 v[72:73], v[72:73], v[160:161]
	v_pk_add_f32 v[94:95], v[148:149], v[162:163]
	v_pk_add_f32 v[148:149], v[150:151], v[216:217]
	v_pk_add_f32 v[150:151], v[154:155], v[164:165]
	v_pk_add_f32 v[154:155], v[236:237], v[248:249]
	v_pk_add_f32 v[76:77], v[76:77], v[158:159]
	v_pk_add_f32 v[74:75], v[240:241], v[74:75]
	v_pk_add_f32 v[160:161], v[168:169], v[188:189]
	v_pk_add_f32 v[162:163], v[170:171], v[190:191]
	v_pk_add_f32 v[164:165], v[176:177], v[224:225]
	v_pk_add_f32 v[168:169], v[178:179], v[184:185]
	v_pk_add_f32 v[170:171], v[180:181], v[210:211]
	v_pk_add_f32 v[84:85], v[182:183], v[84:85]
	v_pk_mul_f32 v[68:69], v[68:69], s[8:9] op_sel_hi:[1,0]
	v_pk_mul_f32 v[66:67], v[66:67], s[8:9] op_sel_hi:[1,0]
	v_pk_mul_f32 v[78:79], v[78:79], s[8:9] op_sel_hi:[1,0]
	v_pk_mul_f32 v[82:83], v[82:83], s[8:9] op_sel_hi:[1,0]
	v_pk_mul_f32 v[132:133], v[132:133], s[8:9] op_sel_hi:[1,0]
	v_pk_mul_f32 v[92:93], v[92:93], s[8:9] op_sel_hi:[1,0]
	v_pk_mul_f32 v[138:139], v[138:139], s[8:9] op_sel_hi:[1,0]
	v_pk_mul_f32 v[140:141], v[140:141], s[8:9] op_sel_hi:[1,0]
	v_pk_mul_f32 v[196:197], v[196:197], s[8:9] op_sel_hi:[1,0]
	v_pk_mul_f32 v[146:147], v[146:147], s[8:9] op_sel_hi:[1,0]
	v_pk_add_f32 v[176:177], v[198:199], v[212:213]
	v_pk_add_f32 v[72:73], v[72:73], v[166:167]
	v_pk_add_f32 v[94:95], v[94:95], v[172:173]
	v_pk_add_f32 v[148:149], v[148:149], v[174:175]
	v_pk_add_f32 v[150:151], v[150:151], v[218:219]
	v_pk_add_f32 v[154:155], v[154:155], v[214:215]
	v_pk_add_f32 v[76:77], v[76:77], v[250:251]
	v_pk_add_f32 v[70:71], v[74:75], v[70:71]
	v_pk_add_f32 v[74:75], v[160:161], v[186:187]
	v_pk_add_f32 v[160:161], v[162:163], v[192:193]
	v_pk_add_f32 v[162:163], v[164:165], v[194:195]
	v_pk_add_f32 v[164:165], v[168:169], v[226:227]
	v_pk_add_f32 v[166:167], v[170:171], v[230:231]
	v_pk_add_f32 v[80:81], v[84:85], v[80:81]
	v_cvt_pk_f32_fp8_e32 v[152:153], v252
	v_pk_mul_f32 v[86:87], v[86:87], s[8:9] op_sel_hi:[1,0]
	v_pk_mul_f32 v[134:135], v[134:135], s[8:9] op_sel_hi:[1,0]
	v_pk_mul_f32 v[136:137], v[136:137], s[8:9] op_sel_hi:[1,0]
	v_pk_add_f32 v[90:91], v[90:91], v[228:229]
	v_pk_add_f32 v[84:85], v[176:177], v[232:233]
	v_pk_fma_f32 v[72:73], v[72:73], s[10:11], v[82:83] op_sel_hi:[1,0,1]
	v_pk_fma_f32 v[78:79], v[94:95], s[10:11], v[78:79] op_sel_hi:[1,0,1]
	v_pk_fma_f32 v[82:83], v[148:149], s[10:11], v[92:93] op_sel_hi:[1,0,1]
	v_pk_fma_f32 v[92:93], v[150:151], s[10:11], v[132:133] op_sel_hi:[1,0,1]
	v_pk_add_f32 v[94:95], v[154:155], v[246:247]
	v_pk_add_f32 v[64:65], v[76:77], v[64:65]
	v_pk_fma_f32 v[74:75], v[74:75], s[10:11], v[140:141] op_sel_hi:[1,0,1]
	v_pk_fma_f32 v[132:133], v[160:161], s[10:11], v[138:139] op_sel_hi:[1,0,1]
	v_pk_fma_f32 v[138:139], v[162:163], s[10:11], v[146:147] op_sel_hi:[1,0,1]
	v_pk_fma_f32 v[140:141], v[164:165], s[10:11], v[196:197] op_sel_hi:[1,0,1]
	v_pk_fma_f32 v[66:67], v[166:167], s[10:11], v[66:67] op_sel_hi:[1,0,1]
	v_pk_fma_f32 v[68:69], v[80:81], s[10:11], v[68:69] op_sel_hi:[1,0,1]
	v_cvt_pk_f32_fp8_sdwa v[156:157], v252 src0_sel:WORD_1
	v_pk_mul_f32 v[88:89], v[88:89], s[8:9] op_sel_hi:[1,0]
	v_pk_add_f32 v[238:239], v[238:239], 0 op_sel_hi:[1,0]
	v_pk_add_f32 v[90:91], v[90:91], v[234:235]
	v_pk_fma_f32 v[80:81], v[84:85], s[10:11], v[86:87] op_sel_hi:[1,0,1]
	v_pk_fma_f32 v[86:87], v[94:95], s[10:11], v[136:137] op_sel_hi:[1,0,1]
	v_pk_fma_f32 v[64:65], v[64:65], s[10:11], v[134:135] op_sel_hi:[1,0,1]
	v_add_f32_e32 v131, v140, v141
	v_add_f32_e32 v134, v138, v139
	v_add_f32_e32 v135, v68, v69
	v_add_f32_e32 v136, v66, v67
	v_pk_add_f32 v[158:159], v[238:239], v[242:243]
	v_pk_fma_f32 v[84:85], v[90:91], s[10:11], v[88:89] op_sel_hi:[1,0,1]
	v_add_f32_e32 v88, v78, v79
	v_add_f32_e32 v89, v72, v73
	v_add_f32_e32 v131, v134, v131
	v_add_f32_e32 v134, v136, v135
	v_pk_add_f32 v[158:159], v[158:159], v[244:245]
	v_add_f32_e32 v88, v89, v88
	v_add_f32_e32 v89, v84, v85
	v_add_f32_e32 v137, v80, v81
	v_add_f32_e32 v134, 0, v134
	v_pk_mul_f32 v[142:143], v[142:143], s[8:9] op_sel_hi:[1,0]
	v_pk_add_f32 v[76:77], v[158:159], v[152:153]
	v_add_f32_e32 v90, v92, v93
	v_add_f32_e32 v91, v82, v83
	v_add_f32_e32 v89, v137, v89
	v_add_f32_e32 v88, v134, v88
	v_pk_mul_f32 v[144:145], v[144:145], s[8:9] op_sel_hi:[1,0]
	v_pk_add_f32 v[70:71], v[70:71], v[156:157]
	v_pk_fma_f32 v[76:77], v[76:77], s[10:11], v[142:143] op_sel_hi:[1,0,1]
	v_add_f32_e32 v90, v91, v90
	v_add_f32_e32 v91, v64, v65
	v_add_f32_e32 v142, v86, v87
	v_add_f32_e32 v88, v88, v89
	v_pk_fma_f32 v[70:71], v[70:71], s[10:11], v[144:145] op_sel_hi:[1,0,1]
	v_add_f32_e32 v94, v132, v133
	v_add_f32_e32 v95, v74, v75
	v_add_f32_e32 v91, v142, v91
	v_add_f32_e32 v88, v88, v90
	v_add_f32_e32 v94, v95, v94
	v_add_f32_e32 v95, v70, v71
	v_add_f32_e32 v143, v76, v77
	v_add_f32_e32 v88, v88, v91
	v_add_f32_e32 v95, v143, v95
	v_add_f32_e32 v88, v88, v94
	v_add_f32_e32 v88, v88, v95
	v_add_f32_e32 v88, v88, v131
	s_nop 1
	v_add_f32_dpp v88, v88, v88 quad_perm:[1,0,3,2] row_mask:0xf bank_mask:0xf bound_ctrl:1
	s_nop 1
	v_add_f32_dpp v88, v88, v88 quad_perm:[2,3,0,1] row_mask:0xf bank_mask:0xf bound_ctrl:1
	s_nop 1
	v_add_f32_dpp v88, v88, v88 row_half_mirror row_mask:0xf bank_mask:0xf bound_ctrl:1
	s_nop 1
	v_add_f32_dpp v88, v88, v88 row_mirror row_mask:0xf bank_mask:0xf bound_ctrl:1
	v_mov_b32_e32 v89, v88
	s_nop 1
	v_permlane16_swap_b32_e32 v88, v89
	v_add_f32_e32 v88, v88, v89
	v_mov_b32_e32 v89, v88
	s_nop 1
	v_permlane32_swap_b32_e32 v88, v89
	v_add_f32_e32 v88, v88, v89
	v_fmac_f32_e32 v69, 0xba000000, v88
	v_fmac_f32_e32 v67, 0xba000000, v88
	v_fmac_f32_e32 v79, 0xba000000, v88
	v_fmac_f32_e32 v73, 0xba000000, v88
	v_fmamk_f32 v68, v88, 0xba000000, v68
	v_fmamk_f32 v66, v88, 0xba000000, v66
	v_fmamk_f32 v78, v88, 0xba000000, v78
	v_fmamk_f32 v72, v88, 0xba000000, v72
	v_fmamk_f32 v84, v88, 0xba000000, v84
	v_fmac_f32_e32 v85, 0xba000000, v88
	v_fmamk_f32 v80, v88, 0xba000000, v80
	v_fmac_f32_e32 v81, 0xba000000, v88
	v_fmamk_f32 v92, v88, 0xba000000, v92
	v_fmac_f32_e32 v93, 0xba000000, v88
	v_fmamk_f32 v82, v88, 0xba000000, v82
	v_fmac_f32_e32 v83, 0xba000000, v88
	v_fmamk_f32 v64, v88, 0xba000000, v64
	v_fmac_f32_e32 v65, 0xba000000, v88
	v_fmamk_f32 v86, v88, 0xba000000, v86
	v_fmac_f32_e32 v87, 0xba000000, v88
	v_fmamk_f32 v132, v88, 0xba000000, v132
	v_fmac_f32_e32 v133, 0xba000000, v88
	v_fmamk_f32 v74, v88, 0xba000000, v74
	v_fmac_f32_e32 v75, 0xba000000, v88
	v_fmamk_f32 v70, v88, 0xba000000, v70
	v_fmac_f32_e32 v71, 0xba000000, v88
	v_fmamk_f32 v76, v88, 0xba000000, v76
	v_fmac_f32_e32 v77, 0xba000000, v88
	v_fmamk_f32 v140, v88, 0xba000000, v140
	v_fmac_f32_e32 v141, 0xba000000, v88
	v_fmamk_f32 v138, v88, 0xba000000, v138
	v_fmac_f32_e32 v139, 0xba000000, v88
	v_mul_f32_e32 v88, v67, v67
	v_mul_f32_e32 v89, v69, v69
	v_mul_f32_e32 v90, v73, v73
	v_mul_f32_e32 v91, v79, v79
	v_mul_f32_e32 v94, v81, v81
	v_mul_f32_e32 v95, v85, v85
	v_fmac_f32_e32 v88, v66, v66
	v_fmac_f32_e32 v89, v68, v68
	v_fmac_f32_e32 v90, v72, v72
	v_fmac_f32_e32 v91, v78, v78
	v_mul_f32_e32 v131, v83, v83
	v_mul_f32_e32 v134, v93, v93
	v_fmac_f32_e32 v94, v80, v80
	v_fmac_f32_e32 v95, v84, v84
	v_add_f32_e32 v88, v88, v89
	v_add_f32_e32 v89, v90, v91
	v_mul_f32_e32 v135, v87, v87
	v_mul_f32_e32 v136, v65, v65
	v_fmac_f32_e32 v131, v82, v82
	v_fmac_f32_e32 v134, v92, v92
	v_add_f32_e32 v90, v94, v95
	v_add_f32_e32 v88, v88, v89
	v_mul_f32_e32 v137, v75, v75
	v_mul_f32_e32 v142, v133, v133
	v_fmac_f32_e32 v135, v86, v86
	v_fmac_f32_e32 v136, v64, v64
	v_add_f32_e32 v91, v131, v134
	v_add_f32_e32 v88, v88, v90
	v_mul_f32_e32 v143, v77, v77
	v_mul_f32_e32 v144, v71, v71
	v_fmac_f32_e32 v137, v74, v74
	v_fmac_f32_e32 v142, v132, v132
	v_add_f32_e32 v94, v135, v136
	v_add_f32_e32 v88, v88, v91
	v_mul_f32_e32 v145, v139, v139
	v_mul_f32_e32 v146, v141, v141
	v_fmac_f32_e32 v143, v76, v76
	v_fmac_f32_e32 v144, v70, v70
	v_add_f32_e32 v95, v137, v142
	v_add_f32_e32 v88, v88, v94
	v_fmac_f32_e32 v145, v138, v138
	v_fmac_f32_e32 v146, v140, v140
	v_add_f32_e32 v131, v143, v144
	v_add_f32_e32 v88, v88, v95
	v_add_f32_e32 v134, v145, v146
	v_add_f32_e32 v88, v88, v131
	v_add_f32_e32 v88, v88, v134
	s_nop 1
	v_add_f32_dpp v88, v88, v88 quad_perm:[1,0,3,2] row_mask:0xf bank_mask:0xf bound_ctrl:1
	s_nop 1
	v_add_f32_dpp v88, v88, v88 quad_perm:[2,3,0,1] row_mask:0xf bank_mask:0xf bound_ctrl:1
	s_nop 1
	v_add_f32_dpp v88, v88, v88 row_half_mirror row_mask:0xf bank_mask:0xf bound_ctrl:1
	s_nop 1
	v_add_f32_dpp v88, v88, v88 row_mirror row_mask:0xf bank_mask:0xf bound_ctrl:1
	v_mov_b32_e32 v89, v88
	s_nop 1
	v_permlane16_swap_b32_e32 v88, v89
	v_add_f32_e32 v88, v88, v89
	v_mov_b32_e32 v89, v88
	s_nop 1
	v_permlane32_swap_b32_e32 v88, v89
	v_add_f32_e32 v88, v88, v89
	v_fmamk_f32 v88, v88, 0x3a000000, v127
	v_mul_f32_e32 v89, 0x4f800000, v88
	v_cmp_gt_f32_e32 vcc, s20, v88
	s_nop 1
	v_cndmask_b32_e32 v88, v88, v89, vcc
	v_sqrt_f32_e32 v89, v88
	s_nop 0
	v_add_u32_e32 v90, -1, v89
	v_add_u32_e32 v91, 1, v89
	v_fma_f32 v94, -v90, v89, v88
	v_fma_f32 v95, -v91, v89, v88
	v_cmp_ge_f32_e64 s[2:3], 0, v94
	s_nop 1
	v_cndmask_b32_e64 v89, v89, v90, s[2:3]
	v_cmp_lt_f32_e64 s[2:3], 0, v95
	s_nop 1
	v_cndmask_b32_e64 v89, v89, v91, s[2:3]
	v_mul_f32_e32 v90, 0x37800000, v89
	v_cndmask_b32_e32 v89, v89, v90, vcc
	v_cmp_class_f32_e32 vcc, v88, v128
	s_nop 1
	v_cndmask_b32_e32 v88, v89, v88, vcc
	v_div_scale_f32 v89, s[2:3], v88, v88, 1.0
	v_rcp_f32_e32 v91, v89
	v_div_scale_f32 v90, vcc, 1.0, v88, 1.0
	v_fma_f32 v94, -v89, v91, 1.0
	v_fmac_f32_e32 v91, v94, v91
	v_mul_f32_e32 v94, v90, v91
	v_fma_f32 v95, -v89, v94, v90
	v_fmac_f32_e32 v94, v95, v91
	v_fma_f32 v89, -v89, v94, v90
	v_div_fmas_f32 v89, v89, v91, v94
	v_div_fixup_f32 v88, v89, v88, 1.0
	v_pk_mul_f32 v[66:67], v[88:89], v[66:67] op_sel_hi:[0,1]
	v_pk_mul_f32 v[68:69], v[88:89], v[68:69] op_sel_hi:[0,1]
	v_pk_mul_f32 v[72:73], v[88:89], v[72:73] op_sel_hi:[0,1]
	v_pk_mul_f32 v[78:79], v[88:89], v[78:79] op_sel_hi:[0,1]
	v_pk_mul_f32 v[80:81], v[88:89], v[80:81] op_sel_hi:[0,1]
	v_pk_mul_f32 v[84:85], v[88:89], v[84:85] op_sel_hi:[0,1]
	v_pk_mul_f32 v[82:83], v[88:89], v[82:83] op_sel_hi:[0,1]
	v_pk_mul_f32 v[90:91], v[88:89], v[92:93] op_sel_hi:[0,1]
	v_pk_mul_f32 v[86:87], v[88:89], v[86:87] op_sel_hi:[0,1]
	v_pk_mul_f32 v[64:65], v[88:89], v[64:65] op_sel_hi:[0,1]
	v_pk_mul_f32 v[74:75], v[88:89], v[74:75] op_sel_hi:[0,1]
	v_pk_mul_f32 v[92:93], v[88:89], v[132:133] op_sel_hi:[0,1]
	v_pk_mul_f32 v[76:77], v[88:89], v[76:77] op_sel_hi:[0,1]
	v_pk_mul_f32 v[70:71], v[88:89], v[70:71] op_sel_hi:[0,1]
	v_pk_mul_f32 v[94:95], v[88:89], v[140:141] op_sel_hi:[0,1]
	v_pk_mul_f32 v[88:89], v[88:89], v[138:139] op_sel_hi:[0,1]
	s_waitcnt lgkmcnt(13)
	v_pk_fma_f32 v[18:19], v[68:69], v[18:19], v[50:51]
	v_pk_fma_f32 v[16:17], v[66:67], v[16:17], v[48:49]
	s_mov_b64 vcc, s[0:1]
	s_waitcnt lgkmcnt(12)
	v_pk_fma_f32 v[2:3], v[78:79], v[2:3], v[34:35]
	v_pk_fma_f32 v[0:1], v[72:73], v[0:1], v[32:33]
	s_waitcnt lgkmcnt(9)
	v_pk_fma_f32 v[22:23], v[84:85], v[22:23], v[54:55]
	v_pk_fma_f32 v[20:21], v[80:81], v[20:21], v[52:53]
	s_waitcnt lgkmcnt(8)
	v_pk_fma_f32 v[6:7], v[90:91], v[6:7], v[38:39]
	v_pk_fma_f32 v[4:5], v[82:83], v[4:5], v[36:37]
	s_waitcnt lgkmcnt(5)
	v_pk_fma_f32 v[26:27], v[64:65], v[26:27], v[58:59]
	v_pk_fma_f32 v[24:25], v[86:87], v[24:25], v[56:57]
	s_waitcnt lgkmcnt(4)
	v_pk_fma_f32 v[10:11], v[92:93], v[10:11], v[42:43]
	v_pk_fma_f32 v[8:9], v[74:75], v[8:9], v[40:41]
	s_waitcnt lgkmcnt(1)
	v_pk_fma_f32 v[30:31], v[70:71], v[30:31], v[62:63]
	v_pk_fma_f32 v[28:29], v[76:77], v[28:29], v[60:61]
	s_waitcnt lgkmcnt(0)
	v_pk_fma_f32 v[12:13], v[88:89], v[12:13], v[44:45]
	v_pk_fma_f32 v[14:15], v[94:95], v[14:15], v[46:47]
	global_store_dwordx4 v[116:117], v[16:19], off nt
	global_store_dwordx4 v[116:117], v[0:3], off offset:1024 nt
	global_store_dwordx4 v[116:117], v[20:23], off offset:2048 nt
	global_store_dwordx4 v[116:117], v[4:7], off offset:3072 nt
	global_store_dwordx4 v[118:119], v[24:27], off nt
	global_store_dwordx4 v[120:121], v[8:11], off nt
	global_store_dwordx4 v[122:123], v[28:31], off nt
	global_store_dwordx4 v[124:125], v[12:15], off nt
	s_cbranch_vccnz .LBB0_1205
